# SGU gelu+norm of v computed once per row in phase B (in place), SGU units copy their head channels to LDS
# baseline (speedup 1.0000x reference)
; #define LAS __attribute__((address_space(3)))
; template <bool MAIN, bool CONV>
; __device__ __forceinline__ void b_row(const Params& p, unsigned char* ws, int l, int row, int lane) {
;     const bf16_t* P = (const bf16_t*)(ws + WS_PA); bf16_t* CAT = (bf16_t*)(ws + WS_CAT);
;     const bf16_t* pr = P + (size_t)row * INP;
;     const bool lat = row < NLAT; const int t = lat ? (row & (SEQ - 1)) : ((row - NLAT) & (CTX - 1)); const int b = lat ? (row >> 11) : ((row - NLAT) >> 8);
;     const int seqlen = lat ? SEQ : CTX;
;     const int c0 = lane * 8; const u32x4 zero4 = (u32x4){0u, 0u, 0u, 0u};
;     u32x4 vq = zero4, vs5 = zero4, ca = zero4, ch = zero4, bg = zero4, pa = zero4, ph = zero4, na = zero4, nh = zero4; u32x2 vkv = (u32x2){0u, 0u}; unsigned short vkr = 0;
;     f32x4 cw0a, cw0b, cw1a, cw1b, cw2a, cw2b, gq0 = (f32x4){0.f, 0.f, 0.f, 0.f}, gq1 = gq0, gkv = gq0; f32x2 rope = (f32x2){1.f, 0.f};
;     cw0a = cw0b = cw1a = cw1b = cw2a = cw2b = gq0;
;     if (MAIN) {
;         if (lane < 48) vq = *(const u32x4*)(pr + C_CQ + lane * 8);
;         vkv = *(const u32x2*)(pr + C_CKV + lane * 4);
;         vkr = pr[C_KR + lane];
;         vs5 = *(const u32x4*)(pr + C_S5 + lane * 8);
;         if (lane < 48) { const float* g = p.in[I_QNG] + l * 384 + lane * 8; gq0 = *(const f32x4*)g; gq1 = *(const f32x4*)(g + 4); }
;         gkv = *(const f32x4*)(p.in[I_KVNG] + l * 256 + lane * 4);
;         if (lat) { const int pos = lane >= 32 ? (t & 63) : (t >> 6); rope = ((const f32x2*)(ws + WS_ROPE))[pos * 16 + (lane & 15)]; }
; __device__ __forceinline__ void ph_rowsplit(const Params& p, int l, LAS unsigned char* lds) {
;     const int tid = opaque_tid(), lane = tid & 63, wave = tid >> 6;
;     unsigned char* ws = opaque_ptr(p.ws);
;     const bf16_t* P = (const bf16_t*)(ws + WS_PA);
;     bf16_t* CAT = (bf16_t*)(ws + WS_CAT);
;     const int nsgu = gridDim.x == 256 ? 0 : ((l == 0) ? B_SGU : 256);
;     const int G_ = (int)gridDim.x, c_ = (int)blockIdx.x, nx = nsgu > G_ ? nsgu - G_ : 0;
;     const bool bal = nx > 0 && nx < G_ && nsgu <= 2 * G_;
;     const int nfew = bal ? 2 * nx : 0;
;     const int nmine = (c_ < nsgu ? 1 : 0) + (c_ < nx ? 1 : 0);
;     int rit = bal ? (c_ < nx ? c_ : nfew + (c_ - nx)) : c_; const int rstride = bal ? (c_ < nx ? nx : G_ - nx) : G_; const int rend = bal ? (c_ < nx ? nfew : B_ROWITEMS) : B_ROWITEMS;
.LBB0_465:
	s_andn2_b64 vcc, exec, s[0:1]
	v_readlane_b32 s0, v252, 5
	v_readlane_b32 s1, v252, 6
	s_mov_b32 s1, s5
	v_writelane_b32 v252, s0, 5
	s_nop 1
	v_writelane_b32 v252, s1, 6
	s_cbranch_vccnz .LBB0_590
	v_readlane_b32 s0, v252, 20
	v_readlane_b32 s1, v252, 21
	s_and_b64 s[0:1], s[0:1], exec
	s_movk_i32 s0, 0x120
	s_cselect_b32 s2, s0, 0x100
	v_readlane_b32 s0, v251, 50
	v_readlane_b32 s1, v251, 51
	s_and_b64 s[0:1], s[0:1], exec
	s_cselect_b32 s4, 0, s2
	s_sub_i32 s0, s4, s94
	s_cmp_gt_i32 s4, s94
	s_cselect_b32 s13, s0, 0
	s_cmp_lt_i32 s13, 1
	s_cselect_b64 s[0:1], -1, 0
	s_cmp_le_i32 s94, s13
	s_cselect_b64 s[2:3], -1, 0
	s_or_b64 s[0:1], s[0:1], s[2:3]
	v_readlane_b32 s2, v253, 18
	s_cmp_gt_u32 s4, s2
	s_cselect_b64 s[2:3], -1, 0
	s_or_b64 s[0:1], s[0:1], s[2:3]
	s_lshl_b32 s14, s13, 1
	s_and_b64 s[2:3], s[0:1], exec
	s_cselect_b32 s14, 0, s14
	s_cmp_lt_i32 s92, s13
	s_cselect_b64 s[2:3], -1, 0
	s_and_b64 s[2:3], s[2:3], exec
	s_cselect_b32 s15, s14, 0x480
	s_sub_i32 s16, s94, s13
	s_cmp_lt_i32 s92, s13
	s_cselect_b64 vcc, -1, 0
	s_and_b64 s[2:3], vcc, exec
	s_cselect_b32 s16, s13, s16
	s_cmp_lt_i32 s92, s4
	s_cselect_b64 s[2:3], -1, 0
	s_waitcnt vmcnt(0)
	v_cndmask_b32_e64 v2, 0, 1, s[2:3]
	v_addc_co_u32_e64 v75, s[2:3], 0, v2, vcc
	s_sub_i32 s4, s92, s13
	s_or_b64 s[2:3], vcc, s[0:1]
	s_add_i32 s4, s4, s14
	s_and_b64 s[2:3], s[2:3], exec
	s_cselect_b32 s31, s92, s4
	s_and_b64 s[0:1], s[0:1], exec
	v_readlane_b32 s2, v252, 5
	s_cselect_b32 s13, s94, s16
	s_cselect_b32 s24, 0x480, s15
	s_lshl_b32 s18, s2, 9
	s_mov_b32 s19, s5
	v_readlane_b32 s52, v251, 16
	s_lshl_b32 s0, s2, 8
	s_lshl_b64 s[14:15], s[18:19], 2
	v_readlane_b32 s56, v251, 20
	s_mul_i32 s4, s2, 0x180
	v_readlane_b32 s57, v251, 21
	s_add_u32 s25, s56, s14
	v_readlane_b32 s62, v251, 26
	s_addc_u32 s26, s57, s15
	s_lshl_b64 s[14:15], s[4:5], 2
	s_mov_b32 s1, s5
	v_readlane_b32 s63, v251, 27
	s_add_u32 s14, s62, s14
	v_readlane_b32 s3, v252, 6
	v_readlane_b32 s66, v251, 30
	s_addc_u32 s15, s63, s15
	s_lshl_b64 s[0:1], s[0:1], 2
	s_mulk_i32 s2, 0x600
	s_mov_b32 s3, s5
	v_readlane_b32 s67, v251, 31
	s_add_u32 s0, s66, s0
	v_readlane_b32 s36, v251, 32
	s_addc_u32 s1, s67, s1
	s_lshl_b64 s[2:3], s[2:3], 2
	v_readlane_b32 s42, v251, 38
	v_readlane_b32 s43, v251, 39
	s_add_u32 s2, s42, s2
	s_addc_u32 s3, s43, s3
	v_mov_b32_e32 v4, v0
	s_mov_b64 s[16:17], 0
	s_add_u32 s20, s84, s16
	v_and_b32_e32 v74, 63, v4
	s_addc_u32 s21, s85, s17
	v_lshlrev_b32_e32 v76, 3, v74
	v_mov_b32_e32 v77, v207
	s_add_u32 s22, s20, 0x1f1b8000
	v_lshl_add_u64 v[2:3], s[20:21], 0, v[76:77]
	s_mov_b64 s[16:17], 0x2fc78000
	v_readlane_b32 s40, v251, 36
	v_readlane_b32 s41, v251, 37
	s_addc_u32 s23, s21, 0
	v_lshl_add_u64 v[80:81], v[2:3], 0, s[16:17]
	v_and_b32_e32 v2, 16, v4
	v_lshlrev_b32_e32 v206, 1, v74
	s_add_u32 s34, s20, 0x3d740000
	v_cmp_eq_u32_e64 s[40:41], 0, v2
	v_lshl_add_u64 v[2:3], s[20:21], 0, v[206:207]
	s_mov_b64 s[16:17], 0x30e78100
	v_ashrrev_i32_e32 v79, 6, v4
	s_addc_u32 s35, s21, 0
	v_and_b32_e32 v89, 15, v4
	v_lshl_add_u64 v[82:83], v[2:3], 0, s[16:17]
	v_bfe_u32 v4, v4, 1, 5
	v_lshlrev_b32_e32 v2, 5, v74
	v_mov_b32_e32 v3, v207
	v_lshlrev_b32_e32 v206, 4, v74
	v_readlane_b32 s37, v251, 33
	v_readlane_b32 s38, v251, 34
	v_readlane_b32 s39, v251, 35
	v_lshl_add_u64 v[84:85], s[14:15], 0, v[2:3]
	s_add_u32 s16, s20, 0x324f8000
	v_mul_u32_u24_e32 v86, 0x300, v4
	v_lshl_add_u64 v[4:5], s[20:21], 0, v[206:207]
	s_mov_b64 s[14:15], 0x2f5b8000
	v_lshl_add_u64 v[92:93], s[0:1], 0, v[206:207]
	v_lshl_add_u64 v[94:95], s[2:3], 0, v[2:3]
	s_mov_b64 s[0:1], 0x1000
	s_mov_b32 s12, 0
	v_cmp_gt_u32_e64 s[36:37], 48, v74
	v_lshlrev_b32_e32 v78, 2, v74
	v_cmp_lt_u32_e64 s[38:39], 31, v74
	s_addc_u32 s17, s21, 0
	v_mov_b32_e32 v87, v207
	v_and_b32_e32 v88, 8, v76
	v_lshl_add_u64 v[90:91], v[4:5], 0, s[14:15]
	v_lshl_add_u64 v[96:97], v[94:95], 0, s[0:1]
	v_readlane_b32 s27, v255, 30
	v_readlane_b32 s53, v251, 17
	v_readlane_b32 s54, v251, 18
	v_readlane_b32 s55, v251, 19
	v_readlane_b32 s58, v251, 22
	v_readlane_b32 s59, v251, 23
	v_readlane_b32 s60, v251, 24
	v_readlane_b32 s61, v251, 25
	v_readlane_b32 s64, v251, 28
	v_readlane_b32 s65, v251, 29
	v_readlane_b32 s44, v251, 40
	v_readlane_b32 s45, v251, 41
	v_readlane_b32 s46, v251, 42
	v_readlane_b32 s47, v251, 43
	v_readlane_b32 s48, v251, 44
	v_readlane_b32 s49, v251, 45
	v_readlane_b32 s50, v251, 46
	v_readlane_b32 s51, v251, 47
	v_readlane_b32 s0, v251, 20
	v_readlane_b32 s1, v251, 21
	v_readlane_b32 s2, v252, 5
	s_nop 1
	s_lshl_b32 s2, s2, 11
	s_add_u32 s0, s0, s2
	s_addc_u32 s1, s1, 0
	v_lshlrev_b32_e32 v188, 5, v74
	global_load_dwordx4 v[180:183], v188, s[0:1]
	global_load_dwordx4 v[184:187], v188, s[0:1] offset:16
	s_branch .LBB0_469
; __device__ __forceinline__ unsigned cvt_pk_bf16(float lo, float hi) { const f32x2 v = {lo, hi}; const bf16x2_t b = __builtin_convertvector(v, bf16x2_t); return __builtin_bit_cast(unsigned, b); }
; __device__ __forceinline__ float bf2f(unsigned short b) { return __uint_as_float(((unsigned)b) << 16); }
; __device__ __forceinline__ float bflo(unsigned w) { return __uint_as_float(w << 16); }
; __device__ __forceinline__ float bfhi(unsigned w) { return __uint_as_float(w & 0xffff0000u); }
; template <bool MAIN, bool CONV>
; __device__ __forceinline__ void b_row(const Params& p, unsigned char* ws, int l, int row, int lane) {
;     ...
;         { const u32x2 v = vkv; const float f0 = bflo(v.x), f1 = bfhi(v.x), f2 = bflo(v.y), f3 = bfhi(v.y);
;           const float ss = wave_sum(f0 * f0 + f1 * f1 + f2 * f2 + f3 * f3); const float rinv = rsqrtf(ss * (1.0f / 256.0f) + EPS);
;           u32x2 w; w.x = cvt_pk_bf16(f0 * rinv * gkv[0], f1 * rinv * gkv[1]); w.y = cvt_pk_bf16(f2 * rinv * gkv[2], f3 * rinv * gkv[3]);
;           *(u32x2*)((bf16_t*)(ws + WS_KVA) + (size_t)row * 256 + lane * 4) = w; }
;         { float v = bf2f(vkr); const float partner = __shfl_xor(v, 16);
.LBB0_467:
	s_or_b64 exec, exec, s[0:1]
	s_waitcnt vmcnt(2)
	v_add_u32_e32 v7, 0xffffe000, v98
	v_ashrrev_i32_e32 v6, 11, v98
	v_lshrrev_b32_e32 v7, 8, v7
	s_waitcnt vmcnt(1)
	v_lshlrev_b32_e32 v14, 16, v24
	v_and_b32_e32 v15, 0xffff0000, v24
	v_cndmask_b32_e64 v26, v7, v6, s[42:43]
	v_lshlrev_b32_e32 v6, 16, v25
	v_and_b32_e32 v7, 0xffff0000, v25
	v_pk_mul_f32 v[16:17], v[14:15], v[14:15]
	v_pk_mul_f32 v[8:9], v[6:7], v[6:7]
	v_add_f32_e32 v16, v16, v17
	v_add_f32_e32 v8, v8, v16
	v_add_f32_e32 v8, v9, v8
	ds_bpermute_b32 v9, v19, v8
	s_mov_b32 s0, 0x800000
	v_and_b32_e32 v27, 0xff, v98
	s_movk_i32 s3, 0x900
	s_movk_i32 s2, 0x180
	s_waitcnt lgkmcnt(0)
	v_add_f32_e32 v8, v8, v9
	ds_bpermute_b32 v9, v18, v8
	s_waitcnt lgkmcnt(0)
	v_add_f32_e32 v8, v8, v9
	ds_bpermute_b32 v9, v20, v8
	s_waitcnt lgkmcnt(0)
	v_add_f32_e32 v8, v8, v9
	ds_bpermute_b32 v9, v21, v8
	s_waitcnt lgkmcnt(0)
	v_add_f32_e32 v8, v8, v9
	ds_bpermute_b32 v9, v35, v8
	s_waitcnt lgkmcnt(0)
	v_add_f32_e32 v8, v8, v9
	ds_bpermute_b32 v9, v36, v8
	s_waitcnt lgkmcnt(0)
	v_add_f32_e32 v8, v8, v9
	v_fmamk_f32 v8, v8, 0x3b800000, v246
	v_cmp_gt_f32_e32 vcc, s0, v8
	v_mul_f32_e32 v9, 0x4b800000, v8
	s_nop 0
	v_cndmask_b32_e32 v8, v8, v9, vcc
	v_rsq_f32_e32 v8, v8
	s_nop 0
	v_mul_f32_e32 v9, 0x45800000, v8
	v_cndmask_b32_e32 v8, v8, v9, vcc
	v_pk_mul_f32 v[14:15], v[8:9], v[14:15] op_sel_hi:[0,1]
	v_pk_mul_f32 v[6:7], v[8:9], v[6:7] op_sel_hi:[0,1]
	s_waitcnt vmcnt(0)
	v_pk_mul_f32 v[10:11], v[10:11], v[14:15]
	v_pk_mul_f32 v[6:7], v[12:13], v[6:7]
	v_cvt_pk_bf16_f32 v10, v10, v11
	v_cvt_pk_bf16_f32 v11, v6, v7
	v_lshlrev_b64 v[6:7], 9, v[98:99]
	v_lshl_add_u64 v[6:7], v[80:81], 0, v[6:7]
	global_store_dwordx2 v[6:7], v[10:11], off
	v_lshlrev_b32_e32 v6, 16, v34
	ds_bpermute_b32 v7, v18, v6
	v_lshlrev_b32_e32 v11, 2, v26
	s_waitcnt lgkmcnt(0)
; __device__ __forceinline__ float bf2f(unsigned short b) { return __uint_as_float(((unsigned)b) << 16); }
; __device__ __forceinline__ float bflo(unsigned w) { return __uint_as_float(w << 16); }
; __device__ __forceinline__ float bfhi(unsigned w) { return __uint_as_float(w & 0xffff0000u); }
; __device__ __forceinline__ unsigned short f2bf(float f) { return (unsigned short)(cvt_pk_bf16(f, 0.f) & 0xffffu); }
; template <bool MAIN, bool CONV>
; __device__ __forceinline__ void b_row(const Params& p, unsigned char* ws, int l, int row, int lane) {
;     ...
;         { float v = bf2f(vkr); const float partner = __shfl_xor(v, 16);
;           if (lat) { const int jj = lane & 31; const float cs = rope.x, sn = rope.y;
;               v = jj < 16 ? (v * cs - partner * sn) : (v * cs + partner * sn); }
;           const int key = lat ? CTX + t : t; const unsigned short o = f2bf(v);
;           bf16_t* kc = (bf16_t*)(ws + WS_KC);
;     #pragma unroll
;           for (int h = 0; h < 4; ++h) kc[((size_t)(b * 4 + h) * NKEY + key) * 192 + 128 + lane] = o; }
;         { const u32x4 v = vs5; const int g = lane >> 1, half = lane & 1;
;           *(u32x4*)((bf16_t*)(ws + WS_UPK) + ((size_t)g * 768 + (row >> 4)) * 512 + (row & 15) * 16 + half * 8) = v; }
; __device__ __forceinline__ void sgu_unit(const Params& p, int l, int un, LAS unsigned char* lds) {
;     ...
;     for (int qi = 0; qi < 16; ++qi) { const int q = wave * 16 + qi;
;         const u32x4 v = vv[qi]; float f[8] = {bflo(v.x), bfhi(v.x), bflo(v.y), bfhi(v.y), bflo(v.z), bfhi(v.z), bflo(v.w), bfhi(v.w)}; float ss = 0.f;
; #pragma unroll
;         for (int j = 0; j < 8; ++j) { f[j] = gelu_tanh(f[j]); ss += f[j] * f[j]; }
;         ss = wave_sum(ss); const float rinv = rsqrtf(ss * (1.0f / 512.0f) + EPS);
;         if ((lane >> 4) == h) { const int c0 = (lane & 15) * 8; const float* g = p.in[I_SGUNG] + l * 512 + h * 128 + c0;
; #pragma unroll
;             for (int j = 0; j < 8; ++j) Vl[(c0 + j) * 136 + q] = f2bf(f[j] * rinv * g[j]); } }
	v_mul_f32_e32 v7, v23, v7
	v_cndmask_b32_e64 v7, v7, -v7, s[40:41]
	v_fmac_f32_e32 v7, v22, v6
	v_cndmask_b32_e64 v6, v6, v7, s[42:43]
	v_add_u32_e32 v7, 0x100, v77
	v_cndmask_b32_e64 v206, v27, v7, s[42:43]
	v_cvt_pk_bf16_f32 v10, v6, s0
	v_mad_i64_i32 v[6:7], s[0:1], v11, s3, v[206:207]
	v_mad_u64_u32 v[8:9], s[0:1], v6, s2, v[82:83]
	v_or_b32_e32 v6, 1, v11
	v_mad_i32_i24 v9, v7, s2, v9
	v_mad_i64_i32 v[6:7], s[0:1], v6, s3, v[206:207]
	global_store_short v[8:9], v10, off
	v_mad_u64_u32 v[8:9], s[0:1], v6, s2, v[82:83]
	v_or_b32_e32 v6, 2, v11
	v_mad_i32_i24 v9, v7, s2, v9
	v_mad_i64_i32 v[6:7], s[0:1], v6, s3, v[206:207]
	global_store_short v[8:9], v10, off
	v_mad_u64_u32 v[8:9], s[0:1], v6, s2, v[82:83]
	v_or_b32_e32 v6, 3, v11
	v_mad_i32_i24 v9, v7, s2, v9
	v_mad_i64_i32 v[6:7], s[0:1], v6, s3, v[206:207]
	global_store_short v[8:9], v10, off
	v_mad_u64_u32 v[8:9], s[0:1], v6, s2, v[82:83]
	v_ashrrev_i32_e32 v6, 4, v98
	v_mad_i32_i24 v9, v7, s2, v9
	v_ashrrev_i32_e32 v7, 31, v6
	v_lshl_add_u64 v[6:7], v[6:7], 0, v[86:87]
	global_store_short v[8:9], v10, off
	v_lshlrev_b64 v[6:7], 10, v[6:7]
	v_lshlrev_b32_e32 v8, 5, v98
	v_lshl_add_u64 v[6:7], s[16:17], 0, v[6:7]
	v_and_b32_e32 v206, 0x1e0, v8
	v_lshl_add_u64 v[6:7], v[6:7], 0, v[206:207]
	v_lshlrev_b32_e32 v206, 1, v88
	v_lshl_add_u64 v[6:7], v[6:7], 0, v[206:207]
	global_store_dwordx4 v[6:7], v[2:5], off
	v_lshlrev_b32_e32 v188, 16, v176
	v_and_b32_e32 v189, 0xffff0000, v176
	v_lshlrev_b32_e32 v190, 16, v177
	v_and_b32_e32 v191, 0xffff0000, v177
	v_lshlrev_b32_e32 v192, 16, v178
	v_and_b32_e32 v193, 0xffff0000, v178
	v_lshlrev_b32_e32 v194, 16, v179
	v_and_b32_e32 v195, 0xffff0000, v179
	v_mul_f32_e32 v196, 0xbdd2d3e8, v188
	v_mul_f32_e32 v197, 0xbdd2d3e8, v189
	v_mul_f32_e32 v198, 0xbdd2d3e8, v190
	v_mul_f32_e32 v199, 0xbdd2d3e8, v191
	v_mul_f32_e32 v200, 0xbdd2d3e8, v192
	v_mul_f32_e32 v201, 0xbdd2d3e8, v193
	v_mul_f32_e32 v202, 0xbdd2d3e8, v194
	v_mul_f32_e32 v203, 0xbdd2d3e8, v195
	v_fmaak_f32 v196, v196, v188, 0xc0135761
	v_fmaak_f32 v197, v197, v189, 0xc0135761
	v_fmaak_f32 v198, v198, v190, 0xc0135761
	v_fmaak_f32 v199, v199, v191, 0xc0135761
	v_fmaak_f32 v200, v200, v192, 0xc0135761
	v_fmaak_f32 v201, v201, v193, 0xc0135761
	v_fmaak_f32 v202, v202, v194, 0xc0135761
	v_fmaak_f32 v203, v203, v195, 0xc0135761
	v_mul_f32_e32 v196, v196, v188
	v_mul_f32_e32 v197, v197, v189
	v_mul_f32_e32 v198, v198, v190
	v_mul_f32_e32 v199, v199, v191
	v_mul_f32_e32 v200, v200, v192
	v_mul_f32_e32 v201, v201, v193
	v_mul_f32_e32 v202, v202, v194
	v_mul_f32_e32 v203, v203, v195
	v_exp_f32_e32 v196, v196
	v_exp_f32_e32 v197, v197
	v_exp_f32_e32 v198, v198
	v_exp_f32_e32 v199, v199
	v_exp_f32_e32 v200, v200
	v_exp_f32_e32 v201, v201
	v_exp_f32_e32 v202, v202
	v_exp_f32_e32 v203, v203
	v_add_f32_e32 v196, 1.0, v196
	v_add_f32_e32 v197, 1.0, v197
	v_add_f32_e32 v198, 1.0, v198
	v_add_f32_e32 v199, 1.0, v199
	v_add_f32_e32 v200, 1.0, v200
	v_add_f32_e32 v201, 1.0, v201
	v_add_f32_e32 v202, 1.0, v202
	v_add_f32_e32 v203, 1.0, v203
	v_rcp_f32_e32 v196, v196
	v_rcp_f32_e32 v197, v197
	v_rcp_f32_e32 v198, v198
	v_rcp_f32_e32 v199, v199
	v_rcp_f32_e32 v200, v200
	v_rcp_f32_e32 v201, v201
	v_rcp_f32_e32 v202, v202
	v_rcp_f32_e32 v203, v203
	v_mul_f32_e32 v188, v196, v188
	v_mul_f32_e32 v189, v197, v189
	v_mul_f32_e32 v190, v198, v190
	v_mul_f32_e32 v191, v199, v191
	v_mul_f32_e32 v192, v200, v192
	v_mul_f32_e32 v193, v201, v193
	v_mul_f32_e32 v194, v202, v194
	v_mul_f32_e32 v195, v203, v195
	v_mul_f32_e32 v196, v189, v189
	v_fmac_f32_e32 v196, v188, v188
	v_fmac_f32_e32 v196, v190, v190
	v_fmac_f32_e32 v196, v191, v191
	v_fmac_f32_e32 v196, v192, v192
	v_fmac_f32_e32 v196, v193, v193
	v_fmac_f32_e32 v196, v194, v194
	v_fmac_f32_e32 v196, v195, v195
	v_mov_b32_e32 v197, v196
	s_nop 1
	v_permlane32_swap_b32_e32 v197, v196
	v_add_f32_e32 v196, v196, v197
	v_mov_b32_e32 v197, v196
	s_nop 1
	v_permlane16_swap_b32_e32 v197, v196
	v_add_f32_e32 v196, v196, v197
	s_nop 1
	v_mov_b32_dpp v197, v196 row_ror:8 row_mask:0xf bank_mask:0xf
	v_add_f32_e32 v196, v196, v197
	s_nop 1
	v_mov_b32_dpp v197, v196 row_shl:4 row_mask:0xf bank_mask:0x5
	v_mov_b32_dpp v197, v196 row_shr:4 row_mask:0xf bank_mask:0xa
	v_add_f32_e32 v196, v196, v197
	s_nop 1
	v_mov_b32_dpp v197, v196 quad_perm:[2,3,0,1] row_mask:0xf bank_mask:0xf
	v_add_f32_e32 v196, v196, v197
	s_nop 1
	v_mov_b32_dpp v197, v196 quad_perm:[1,0,3,2] row_mask:0xf bank_mask:0xf
	v_add_f32_e32 v196, v196, v197
	v_fmamk_f32 v196, v196, 0x3b000000, v246
	v_cmp_gt_f32_e32 vcc, 0x800000, v196
	v_mul_f32_e32 v197, 0x4b800000, v196
	s_nop 1
	v_cndmask_b32_e32 v196, v196, v197, vcc
	s_nop 0
	v_rsq_f32_e32 v196, v196
	s_nop 1
	v_mul_f32_e32 v197, 0x45800000, v196
	v_cndmask_b32_e32 v196, v196, v197, vcc
	v_mul_f32_e32 v188, v188, v196
	v_mul_f32_e32 v189, v189, v196
	v_mul_f32_e32 v190, v190, v196
	v_mul_f32_e32 v191, v191, v196
	v_mul_f32_e32 v192, v192, v196
	v_mul_f32_e32 v193, v193, v196
	v_mul_f32_e32 v194, v194, v196
	v_mul_f32_e32 v195, v195, v196
	v_mul_f32_e32 v188, v188, v180
	v_mul_f32_e32 v189, v189, v181
	v_mul_f32_e32 v190, v190, v182
	v_mul_f32_e32 v191, v191, v183
	v_mul_f32_e32 v192, v192, v184
	v_mul_f32_e32 v193, v193, v185
	v_mul_f32_e32 v194, v194, v186
	v_mul_f32_e32 v195, v195, v187
	v_cvt_pk_bf16_f32 v176, v188, v189
	v_cvt_pk_bf16_f32 v177, v190, v191
	v_cvt_pk_bf16_f32 v178, v192, v193
	v_cvt_pk_bf16_f32 v179, v194, v195
	global_store_dwordx4 v[204:205], v[176:179], off offset:1024

; template <bool MAIN, bool CONV>
; __device__ __forceinline__ void b_row(const Params& p, unsigned char* ws, int l, int row, int lane) {
;     ...
;     if (MAIN) {
;         if (lane < 48) vq = *(const u32x4*)(pr + C_CQ + lane * 8);
; __device__ __forceinline__ void sgu_unit(const Params& p, int l, int un, LAS unsigned char* lds) {
;     ...
;     for (int qi = 0; qi < 16; ++qi) vv[qi] = *(const u32x4*)(P + (size_t)(row0 + wave * 16 + qi) * INP + C_SGU_V + lane * 8);
.LBB0_528:
	s_and_b64 vcc, exec, s[0:1]
	s_cbranch_vccz .LBB0_468
	v_lshlrev_b32_e32 v204, 4, v74
	v_mov_b32_e32 v205, v207
	v_lshl_add_u64 v[204:205], v[100:101], 0, v[204:205]
	global_load_dwordx4 v[176:179], v[204:205], off offset:1024
	v_mov_b32_e32 v6, 0
	v_lshlrev_b32_e32 v2, 1, v76
	v_mov_b32_e32 v18, 0
	v_mov_b32_e32 v19, 0
	v_mov_b32_e32 v20, 0
	v_mov_b32_e32 v21, 0
	s_and_saveexec_b64 s[0:1], s[36:37]
	s_cbranch_execz .LBB0_531
	v_mov_b32_e32 v3, v207
	v_lshl_add_u64 v[4:5], v[100:101], 0, v[2:3]
	global_load_dwordx4 v[18:21], v[4:5], off offset:2048

; #define LAS __attribute__((address_space(3)))
; __device__ __forceinline__ int opaque_tid() { int t = threadIdx.x; asm volatile("" : "+v"(t)); return t; }
; __device__ __forceinline__ unsigned char* opaque_ptr(unsigned char* q) { long z = 0; asm volatile("" : "+s"(z)); return q + z; }
;     __device__ __forceinline__ void init(const void* A_, const void* B_, int G_, int c_) { T.init(A_, B_, DM, DM, NLAT / 256, INP / 256, 1, 0, 0, G_, c_, 0); }
; __device__ __forceinline__ void sgu_unit(const Params& p, int l, int un, LAS unsigned char* lds) {
;     const int tid = opaque_tid(), lane = tid & 63, wave = tid >> 6;
;     unsigned char* ws = opaque_ptr(p.ws);
;     const bf16_t* P = (const bf16_t*)(ws + WS_PA);
;     bf16_t* CAT = (bf16_t*)(ws + WS_CAT);
;     const int cc = un >> 2, h = un & 3; const int row0 = cc * 128;
;     LAS bf16_t* Wl = (LAS bf16_t*)lds;
;     LAS bf16_t* Vl = (LAS bf16_t*)(lds + 128 * 136 * 2);
;     const float* Wg = p.in[I_SGUW] + ((size_t)l * 4 + h) * 128 * 128;
;     f32x4 wq[8]; u32x4 vv[16];
; #pragma unroll
;     for (int i = 0; i < 8; ++i) wq[i] = *(const f32x4*)(Wg + (i * 512 + tid) * 4);
; #pragma unroll
;     for (int qi = 0; qi < 16; ++qi) vv[qi] = *(const u32x4*)(P + (size_t)(row0 + wave * 16 + qi) * INP + C_SGU_V + lane * 8);
; __global__ void __launch_bounds__(512, 2) fwd(Params p) {
;     ...
;             { pg8::TileSched S; S.init(ws + WS_UPK, (bf16_t*)(ws + WS_G2B) + (size_t)l * 32 * 256 * 512, 512, 512, 3, 1, 32, (size_t)768 * 512 * 2, (size_t)256 * 512 * 2, G, c, (l == 0 && G == 256) ? 32 : 0);
;               pg8::EpiS2 E{(bf16_t*)(ws + WS_GB)};
;               pg8::Unit u0; if (S.next(0, u0)) { carry_wait(p, l); pg8::gemm_phase(lds, pg8::Desc{512, 512, 512}, S, E); }
;               else if (G == 256) { const int un = c - (l == 0 ? 128 : 96); if (un >= 0) sgu_unit(p, l, un, lds); } }
.LBB0_1258:
	v_readlane_b32 s0, v251, 50
	v_readlane_b32 s2, v252, 20
	v_readlane_b32 s1, v251, 51
	v_readlane_b32 s3, v252, 21
	s_and_b64 s[0:1], s[0:1], s[2:3]
	s_and_b64 s[0:1], s[0:1], exec
	s_cselect_b32 s0, 32, 0
	v_readlane_b32 s2, v255, 11
	s_mul_hi_u32 s1, s0, s2
	v_readlane_b32 s3, v255, 12
	s_mul_i32 s1, s1, s3
	s_sub_i32 s0, s0, s1
	s_sub_i32 s1, s0, s3
	s_cmp_ge_u32 s0, s3
	s_cselect_b32 s0, s1, s0
	s_sub_i32 s1, s0, s3
	s_cmp_ge_u32 s0, s3
	s_cselect_b32 s0, s1, s0
	v_readlane_b32 s1, v255, 42
	s_sub_i32 s0, s1, s0
	s_ashr_i32 s1, s0, 31
	s_abs_i32 s0, s0
	s_mul_hi_u32 s2, s0, s2
	s_mul_i32 s2, s2, s3
	s_sub_i32 s0, s0, s2
	s_sub_i32 s2, s0, s3
	s_cmp_ge_u32 s0, s3
	s_cselect_b32 s0, s2, s0
	s_sub_i32 s2, s0, s3
	s_cmp_ge_u32 s0, s3
	s_cselect_b32 s0, s2, s0
	s_xor_b32 s0, s0, s1
	s_sub_i32 s26, s0, s1
	s_cmpk_gt_i32 s26, 0x5f
	s_mov_b64 s[0:1], -1
	s_barrier
	s_cbranch_scc0 .LBB0_1294
	v_readlane_b32 s0, v252, 20
	v_readlane_b32 s1, v252, 21
	s_and_b64 s[0:1], s[0:1], exec
	s_movk_i32 s0, 0xff80
	s_cselect_b32 s0, s0, 0xffffffa0
	s_add_i32 s0, s0, s92
	v_readlane_b32 s12, v251, 50
	s_cmp_lt_i32 s0, 0
	v_readlane_b32 s13, v251, 51
	s_cselect_b64 s[2:3], -1, 0
	s_xor_b64 s[12:13], s[12:13], -1
	s_or_b64 s[2:3], s[2:3], s[12:13]
	s_and_b64 vcc, exec, s[2:3]
	s_cbranch_vccnz .LBB0_1293
	v_readlane_b32 s2, v252, 5
	v_readlane_b32 s44, v251, 16
	s_lshl_b32 s1, s0, 5
	s_lshl_b32 s0, s2, 9
	v_readlane_b32 s2, v253, 39
	v_readlane_b32 s48, v251, 20
	v_readlane_b32 s49, v251, 21
	v_readlane_b32 s3, v252, 6
	s_or_b32 s40, s0, s2
	s_mov_b32 s41, s5
	v_readlane_b32 s50, v251, 22
	v_readlane_b32 s51, v251, 23
	v_readlane_b32 s52, v251, 24
	v_readlane_b32 s53, v251, 25
	v_readlane_b32 s54, v251, 26
	v_readlane_b32 s55, v251, 27
	s_mov_b64 s[12:13], s[48:49]
	s_lshl_b64 s[2:3], s[40:41], 9
	s_mov_b64 s[14:15], s[50:51]
	v_mov_b32_e32 v64, v0
	s_add_u32 s2, s14, s2
	s_addc_u32 s3, s15, s3
	v_lshlrev_b32_e32 v2, 2, v64
	v_ashrrev_i32_e32 v3, 31, v2
	v_add_u32_e32 v62, 0x800, v2
	s_mov_b64 s[14:15], 0
	v_lshl_add_u64 v[4:5], v[2:3], 2, s[2:3]
	v_ashrrev_i32_e32 v63, 31, v62
	v_lshl_add_u64 v[6:7], v[62:63], 2, s[2:3]
	global_load_dwordx4 v[66:69], v[4:5], off
	global_load_dwordx4 v[70:73], v[6:7], off
	v_add_u32_e32 v102, 0x1000, v2
	v_ashrrev_i32_e32 v103, 31, v102
	v_add_u32_e32 v104, 0x1800, v2
	v_lshl_add_u64 v[4:5], v[102:103], 2, s[2:3]
	v_ashrrev_i32_e32 v105, 31, v104
	s_and_b32 s12, s1, 0x7fffff80
	s_mov_b32 s1, s5
	v_lshl_add_u64 v[6:7], v[104:105], 2, s[2:3]
	global_load_dwordx4 v[74:77], v[4:5], off
	global_load_dwordx4 v[78:81], v[6:7], off
	s_lshl_b64 s[0:1], s[0:1], 2
	v_readlane_b32 s13, v253, 41
	v_add_u32_e32 v106, 0x2000, v2
	s_add_u32 s0, s13, s0
	v_readlane_b32 s13, v253, 42
	v_ashrrev_i32_e32 v107, 31, v106
	v_add_u32_e32 v108, 0x2800, v2
	s_addc_u32 s1, s13, s1
	v_lshl_add_u64 v[4:5], v[106:107], 2, s[2:3]
	v_ashrrev_i32_e32 v109, 31, v108
	s_add_u32 s36, s84, s14
	v_lshl_add_u64 v[6:7], v[108:109], 2, s[2:3]
	global_load_dwordx4 v[82:85], v[4:5], off
	global_load_dwordx4 v[86:89], v[6:7], off
	s_addc_u32 s37, s85, s15
	v_add_u32_e32 v110, 0x3000, v2
	v_add_u32_e32 v112, 0x3800, v2
	s_add_u32 s38, s36, 0x1f1b8000
	v_ashrrev_i32_e32 v111, 31, v110
	v_ashrrev_i32_e32 v113, 31, v112
	v_ashrrev_i32_e32 v103, 6, v64
	s_addc_u32 s39, s37, 0
	v_lshl_add_u64 v[4:5], v[110:111], 2, s[2:3]
	v_lshl_add_u64 v[2:3], v[112:113], 2, s[2:3]
	v_lshlrev_b32_e32 v65, 4, v103
	v_and_b32_e32 v8, 63, v64
	global_load_dwordx4 v[90:93], v[4:5], off
	global_load_dwordx4 v[94:97], v[2:3], off
	v_add_u32_e32 v9, s12, v65
	v_mov_b64_e32 v[2:3], s[38:39]
	s_movk_i32 s13, 0x1e00
	v_mad_i64_i32 v[4:5], s[2:3], v9, s13, v[2:3]
	v_lshlrev_b32_e32 v206, 4, v8
	v_or_b32_e32 v6, 1, v9
	v_lshl_add_u64 v[4:5], v[4:5], 0, v[206:207]
	v_mad_i64_i32 v[6:7], s[2:3], v6, s13, v[2:3]
	v_lshl_add_u64 v[6:7], v[6:7], 0, v[206:207]
	global_load_dwordx4 v[98:101], v[4:5], off offset:1024
	global_load_dwordx4 v[58:61], v[6:7], off offset:1024
	v_or_b32_e32 v4, 2, v9
	v_or_b32_e32 v6, 3, v9
	v_mad_i64_i32 v[4:5], s[2:3], v4, s13, v[2:3]
	v_mad_i64_i32 v[6:7], s[2:3], v6, s13, v[2:3]
	v_lshl_add_u64 v[4:5], v[4:5], 0, v[206:207]
	v_lshl_add_u64 v[6:7], v[6:7], 0, v[206:207]
	global_load_dwordx4 v[54:57], v[4:5], off offset:1024
	global_load_dwordx4 v[50:53], v[6:7], off offset:1024
	v_or_b32_e32 v4, 4, v9
	v_or_b32_e32 v6, 5, v9
	v_mad_i64_i32 v[4:5], s[2:3], v4, s13, v[2:3]
	v_mad_i64_i32 v[6:7], s[2:3], v6, s13, v[2:3]
	v_lshl_add_u64 v[4:5], v[4:5], 0, v[206:207]
	v_lshl_add_u64 v[6:7], v[6:7], 0, v[206:207]
	global_load_dwordx4 v[46:49], v[4:5], off offset:1024
	global_load_dwordx4 v[42:45], v[6:7], off offset:1024
	v_or_b32_e32 v4, 6, v9
	v_or_b32_e32 v6, 7, v9
	v_mad_i64_i32 v[4:5], s[2:3], v4, s13, v[2:3]
	v_mad_i64_i32 v[6:7], s[2:3], v6, s13, v[2:3]
	v_lshl_add_u64 v[4:5], v[4:5], 0, v[206:207]
	v_lshl_add_u64 v[6:7], v[6:7], 0, v[206:207]
	global_load_dwordx4 v[38:41], v[4:5], off offset:1024
	global_load_dwordx4 v[34:37], v[6:7], off offset:1024
	v_or_b32_e32 v4, 8, v9
	v_or_b32_e32 v6, 9, v9
	v_mad_i64_i32 v[4:5], s[2:3], v4, s13, v[2:3]
	v_mad_i64_i32 v[6:7], s[2:3], v6, s13, v[2:3]
	v_lshl_add_u64 v[4:5], v[4:5], 0, v[206:207]
	v_lshl_add_u64 v[6:7], v[6:7], 0, v[206:207]
	global_load_dwordx4 v[30:33], v[4:5], off offset:1024
	global_load_dwordx4 v[26:29], v[6:7], off offset:1024
	v_or_b32_e32 v4, 10, v9
	v_or_b32_e32 v6, 11, v9
	v_mad_i64_i32 v[4:5], s[2:3], v4, s13, v[2:3]
	v_mad_i64_i32 v[6:7], s[2:3], v6, s13, v[2:3]
	v_lshl_add_u64 v[4:5], v[4:5], 0, v[206:207]
	v_lshl_add_u64 v[6:7], v[6:7], 0, v[206:207]
	global_load_dwordx4 v[22:25], v[4:5], off offset:1024
	global_load_dwordx4 v[18:21], v[6:7], off offset:1024
	v_or_b32_e32 v4, 12, v9
	v_or_b32_e32 v6, 13, v9
	v_mad_i64_i32 v[4:5], s[2:3], v4, s13, v[2:3]
	v_mad_i64_i32 v[6:7], s[2:3], v6, s13, v[2:3]
	v_lshl_add_u64 v[4:5], v[4:5], 0, v[206:207]
	v_lshl_add_u64 v[6:7], v[6:7], 0, v[206:207]
	v_lshlrev_b32_e32 v105, 3, v64
	global_load_dwordx4 v[14:17], v[4:5], off offset:1024
	global_load_dwordx4 v[10:13], v[6:7], off offset:1024
	v_or_b32_e32 v4, 14, v9
	v_or_b32_e32 v6, 15, v9
	v_and_b32_e32 v63, 0xf8, v105
	v_mad_i64_i32 v[4:5], s[2:3], v4, s13, v[2:3]
	v_mad_i64_i32 v[2:3], s[2:3], v6, s13, v[2:3]
	v_add_u32_e32 v114, 0, v63
	v_bfe_i32 v63, v64, 5, 25
	s_movk_i32 s13, 0x110
	v_lshl_add_u64 v[4:5], v[4:5], 0, v[206:207]
	v_lshl_add_u64 v[2:3], v[2:3], 0, v[206:207]
	s_waitcnt vmcnt(21)
; #define LAS __attribute__((address_space(3)))
; __device__ __forceinline__ unsigned cvt_pk_bf16(float lo, float hi) { const f32x2 v = {lo, hi}; const bf16x2_t b = __builtin_convertvector(v, bf16x2_t); return __builtin_bit_cast(unsigned, b); }
; __device__ __forceinline__ float bflo(unsigned w) { return __uint_as_float(w << 16); }
; __device__ __forceinline__ float bfhi(unsigned w) { return __uint_as_float(w & 0xffff0000u); }
; __device__ __forceinline__ unsigned short f2bf(float f) { return (unsigned short)(cvt_pk_bf16(f, 0.f) & 0xffffu); }
; __device__ __forceinline__ void sgu_unit(const Params& p, int l, int un, LAS unsigned char* lds) {
;     ...
;     f32x4 wq[8]; u32x4 vv[16];
; #pragma unroll
;     for (int i = 0; i < 8; ++i) wq[i] = *(const f32x4*)(Wg + (i * 512 + tid) * 4);
; #pragma unroll
;     for (int qi = 0; qi < 16; ++qi) vv[qi] = *(const u32x4*)(P + (size_t)(row0 + wave * 16 + qi) * INP + C_SGU_V + lane * 8);
; #pragma unroll
;     for (int i = 0; i < 8; ++i) { const int e4 = (i * 512 + tid) * 4, r = e4 >> 7, c = e4 & 127; const f32x4 v = wq[i];
;         u32x2 w; w.x = cvt_pk_bf16(v[0], v[1]); w.y = cvt_pk_bf16(v[2], v[3]); *(LAS u32x2*)(Wl + r * 136 + c) = w; }
; #pragma unroll
;     for (int qi = 0; qi < 16; ++qi) { const int q = wave * 16 + qi;
;         const u32x4 v = vv[qi]; float f[8] = {bflo(v.x), bfhi(v.x), bflo(v.y), bfhi(v.y), bflo(v.z), bfhi(v.z), bflo(v.w), bfhi(v.w)}; float ss = 0.f;
; #pragma unroll
;         for (int j = 0; j < 8; ++j) { f[j] = gelu_tanh(f[j]); ss += f[j] * f[j]; }
;         ss = wave_sum(ss); const float rinv = rsqrtf(ss * (1.0f / 512.0f) + EPS);
;         if ((lane >> 4) == h) { const int c0 = (lane & 15) * 8; const float* g = p.in[I_SGUNG] + l * 512 + h * 128 + c0;
; #pragma unroll
;             for (int j = 0; j < 8; ++j) Vl[(c0 + j) * 136 + q] = f2bf(f[j] * rinv * g[j]); } }
	v_cvt_pk_bf16_f32 v66, v66, v67
	v_cvt_pk_bf16_f32 v67, v68, v69
	v_mad_u64_u32 v[68:69], s[2:3], v63, s13, v[114:115]
	global_load_dwordx4 v[6:9], v[4:5], off offset:1024
	s_nop 0
	global_load_dwordx4 v[2:5], v[2:3], off offset:1024
	ds_write_b64 v68, v[66:67]
	v_ashrrev_i32_e32 v66, 7, v62
	s_waitcnt vmcnt(22)
	v_cvt_pk_bf16_f32 v62, v70, v71
	v_cvt_pk_bf16_f32 v63, v72, v73
	v_mad_u64_u32 v[66:67], s[2:3], v66, s13, v[114:115]
	ds_write_b64 v66, v[62:63]
	v_ashrrev_i32_e32 v66, 7, v102
	s_waitcnt vmcnt(21)
	v_cvt_pk_bf16_f32 v62, v74, v75
	v_cvt_pk_bf16_f32 v63, v76, v77
	v_mad_u64_u32 v[66:67], s[2:3], v66, s13, v[114:115]
	ds_write_b64 v66, v[62:63]
	v_ashrrev_i32_e32 v66, 7, v104
	s_waitcnt vmcnt(20)
	v_cvt_pk_bf16_f32 v62, v78, v79
	v_cvt_pk_bf16_f32 v63, v80, v81
	v_mad_u64_u32 v[66:67], s[2:3], v66, s13, v[114:115]
	ds_write_b64 v66, v[62:63]
	v_ashrrev_i32_e32 v66, 7, v106
	s_waitcnt vmcnt(19)
	v_cvt_pk_bf16_f32 v62, v82, v83
	v_cvt_pk_bf16_f32 v63, v84, v85
	v_mad_u64_u32 v[66:67], s[2:3], v66, s13, v[114:115]
	ds_write_b64 v66, v[62:63]
	v_ashrrev_i32_e32 v66, 7, v108
	s_waitcnt vmcnt(18)
	v_cvt_pk_bf16_f32 v62, v86, v87
	v_cvt_pk_bf16_f32 v63, v88, v89
	v_mad_u64_u32 v[66:67], s[2:3], v66, s13, v[114:115]
	ds_write_b64 v66, v[62:63]
	v_ashrrev_i32_e32 v66, 7, v110
	s_waitcnt vmcnt(17)
	v_cvt_pk_bf16_f32 v62, v90, v91
	v_cvt_pk_bf16_f32 v63, v92, v93
	v_mad_u64_u32 v[66:67], s[2:3], v66, s13, v[114:115]
	ds_write_b64 v66, v[62:63]
	v_ashrrev_i32_e32 v66, 7, v112
	v_mad_u64_u32 v[66:67], s[2:3], v66, s13, v[114:115]
	s_waitcnt vmcnt(15)
	v_cvt_pk_bf16_f32 v62, v94, v95
	v_cvt_pk_bf16_f32 v63, v96, v97
	ds_write_b64 v66, v[62:63]
	v_and_b32_e32 v62, 64, v249
	v_add_u32_e32 v62, 64, v62
	v_xor_b32_e32 v63, 32, v249
	v_cmp_lt_i32_e32 vcc, v63, v62
	v_cndmask_b32_e32 v63, v249, v63, vcc
	v_lshlrev_b32_e32 v68, 2, v63
	v_and_b32_e32 v84, 0x78, v105
	v_readlane_b32 s2, v253, 40
	v_lshlrev_b32_e32 v206, 2, v84
	v_readlane_b32 s45, v251, 17
	v_readlane_b32 s46, v251, 18
	v_readlane_b32 s47, v251, 19
	v_readlane_b32 s56, v251, 28
	v_readlane_b32 s57, v251, 29
	v_readlane_b32 s58, v251, 30
	v_readlane_b32 s59, v251, 31
	v_bfe_u32 v66, v64, 4, 2
	v_cmp_eq_u32_e32 vcc, s2, v66
	s_mov_b64 s[16:17], s[52:53]
	v_lshl_add_u32 v67, v103, 5, 0
	v_lshl_add_u64 v[62:63], s[0:1], 0, v[206:207]
	v_mad_u32_u24 v67, v84, s13, v67
	v_lshrrev_b32_e32 v170, 6, v0
	v_lshlrev_b32_e32 v170, 1, v170
	v_and_b32_e32 v171, 15, v0
	v_xor_b32_e32 v168, v170, v171
	v_sub_u32_e32 v168, v168, v170
	v_lshl_add_u32 v168, v168, 4, v67
	v_or_b32_e32 v170, 1, v170
	v_xor_b32_e32 v169, v170, v171
	v_sub_u32_e32 v169, v169, v170
	v_lshl_add_u32 v169, v169, 4, v67
	s_mov_b64 s[18:19], s[54:55]
	s_and_saveexec_b64 s[0:1], vcc
	s_cbranch_execz .LBB0_1262
	ds_write_b16 v168, v98 offset:34816
	ds_write_b16_d16_hi v168, v98 offset:35088
	ds_write_b16 v168, v99 offset:35360
	ds_write_b16_d16_hi v168, v99 offset:35632
	ds_write_b16 v168, v100 offset:35904
	ds_write_b16_d16_hi v168, v100 offset:36176
	ds_write_b16 v168, v101 offset:36448
	ds_write_b16_d16_hi v168, v101 offset:36720
.LBB0_1262:
	s_or_b64 exec, exec, s[0:1]
	s_waitcnt vmcnt(14)
	s_and_saveexec_b64 s[0:1], vcc
	s_cbranch_execz .LBB0_1264
	ds_write_b16 v168, v58 offset:34818
	ds_write_b16_d16_hi v168, v58 offset:35090
	ds_write_b16 v168, v59 offset:35362
	ds_write_b16_d16_hi v168, v59 offset:35634
	ds_write_b16 v168, v60 offset:35906
	ds_write_b16_d16_hi v168, v60 offset:36178
	ds_write_b16 v168, v61 offset:36450
	ds_write_b16_d16_hi v168, v61 offset:36722
.LBB0_1264:
	s_or_b64 exec, exec, s[0:1]
	s_waitcnt vmcnt(13)
	s_and_saveexec_b64 s[0:1], vcc
	s_cbranch_execz .LBB0_1266
	ds_write_b16 v168, v54 offset:34820
	ds_write_b16_d16_hi v168, v54 offset:35092
	ds_write_b16 v168, v55 offset:35364
	ds_write_b16_d16_hi v168, v55 offset:35636
	ds_write_b16 v168, v56 offset:35908
	ds_write_b16_d16_hi v168, v56 offset:36180
	ds_write_b16 v168, v57 offset:36452
	ds_write_b16_d16_hi v168, v57 offset:36724
.LBB0_1266:
	s_or_b64 exec, exec, s[0:1]
	s_waitcnt vmcnt(12)
	s_and_saveexec_b64 s[0:1], vcc
	s_cbranch_execz .LBB0_1268
	ds_write_b16 v168, v50 offset:34822
	ds_write_b16_d16_hi v168, v50 offset:35094
	ds_write_b16 v168, v51 offset:35366
	ds_write_b16_d16_hi v168, v51 offset:35638
	ds_write_b16 v168, v52 offset:35910
	ds_write_b16_d16_hi v168, v52 offset:36182
	ds_write_b16 v168, v53 offset:36454
	ds_write_b16_d16_hi v168, v53 offset:36726
.LBB0_1268:
	s_or_b64 exec, exec, s[0:1]
	s_waitcnt vmcnt(11)
	s_and_saveexec_b64 s[0:1], vcc
	s_cbranch_execz .LBB0_1270
	ds_write_b16 v168, v46 offset:34824
	ds_write_b16_d16_hi v168, v46 offset:35096
	ds_write_b16 v168, v47 offset:35368
	ds_write_b16_d16_hi v168, v47 offset:35640
	ds_write_b16 v168, v48 offset:35912
	ds_write_b16_d16_hi v168, v48 offset:36184
	ds_write_b16 v168, v49 offset:36456
	ds_write_b16_d16_hi v168, v49 offset:36728
; __device__ __forceinline__ float bflo(unsigned w) { return __uint_as_float(w << 16); }
; __device__ __forceinline__ float bfhi(unsigned w) { return __uint_as_float(w & 0xffff0000u); }
; __device__ __forceinline__ unsigned short f2bf(float f) { return (unsigned short)(cvt_pk_bf16(f, 0.f) & 0xffffu); }
; __device__ __forceinline__ void sgu_unit(const Params& p, int l, int un, LAS unsigned char* lds) {
;     ...
;     for (int qi = 0; qi < 16; ++qi) { const int q = wave * 16 + qi;
;         const u32x4 v = vv[qi]; float f[8] = {bflo(v.x), bfhi(v.x), bflo(v.y), bfhi(v.y), bflo(v.z), bfhi(v.z), bflo(v.w), bfhi(v.w)}; float ss = 0.f;
; #pragma unroll
;         for (int j = 0; j < 8; ++j) { f[j] = gelu_tanh(f[j]); ss += f[j] * f[j]; }
;         ss = wave_sum(ss); const float rinv = rsqrtf(ss * (1.0f / 512.0f) + EPS);
;         if ((lane >> 4) == h) { const int c0 = (lane & 15) * 8; const float* g = p.in[I_SGUNG] + l * 512 + h * 128 + c0;
; #pragma unroll
;             for (int j = 0; j < 8; ++j) Vl[(c0 + j) * 136 + q] = f2bf(f[j] * rinv * g[j]); } }
.LBB0_1270:
	s_or_b64 exec, exec, s[0:1]
	s_waitcnt vmcnt(10)
	s_and_saveexec_b64 s[0:1], vcc
	s_cbranch_execz .LBB0_1272
	ds_write_b16 v168, v42 offset:34826
	ds_write_b16_d16_hi v168, v42 offset:35098
	ds_write_b16 v168, v43 offset:35370
	ds_write_b16_d16_hi v168, v43 offset:35642
	ds_write_b16 v168, v44 offset:35914
	ds_write_b16_d16_hi v168, v44 offset:36186
	ds_write_b16 v168, v45 offset:36458
	ds_write_b16_d16_hi v168, v45 offset:36730
.LBB0_1272:
	s_or_b64 exec, exec, s[0:1]
	s_waitcnt vmcnt(9)
	s_and_saveexec_b64 s[0:1], vcc
	s_cbranch_execz .LBB0_1274
	ds_write_b16 v168, v38 offset:34828
	ds_write_b16_d16_hi v168, v38 offset:35100
	ds_write_b16 v168, v39 offset:35372
	ds_write_b16_d16_hi v168, v39 offset:35644
	ds_write_b16 v168, v40 offset:35916
	ds_write_b16_d16_hi v168, v40 offset:36188
	ds_write_b16 v168, v41 offset:36460
	ds_write_b16_d16_hi v168, v41 offset:36732
.LBB0_1274:
	s_or_b64 exec, exec, s[0:1]
	s_waitcnt vmcnt(8)
	s_and_saveexec_b64 s[0:1], vcc
	s_cbranch_execz .LBB0_1276
	ds_write_b16 v168, v34 offset:34830
	ds_write_b16_d16_hi v168, v34 offset:35102
	ds_write_b16 v168, v35 offset:35374
	ds_write_b16_d16_hi v168, v35 offset:35646
	ds_write_b16 v168, v36 offset:35918
	ds_write_b16_d16_hi v168, v36 offset:36190
	ds_write_b16 v168, v37 offset:36462
	ds_write_b16_d16_hi v168, v37 offset:36734
.LBB0_1276:
	s_or_b64 exec, exec, s[0:1]
	s_waitcnt vmcnt(7)
	s_and_saveexec_b64 s[0:1], vcc
	s_cbranch_execz .LBB0_1278
	ds_write_b16 v169, v30 offset:34832
	ds_write_b16_d16_hi v169, v30 offset:35104
	ds_write_b16 v169, v31 offset:35376
	ds_write_b16_d16_hi v169, v31 offset:35648
	ds_write_b16 v169, v32 offset:35920
	ds_write_b16_d16_hi v169, v32 offset:36192
	ds_write_b16 v169, v33 offset:36464
	ds_write_b16_d16_hi v169, v33 offset:36736
.LBB0_1278:
	s_or_b64 exec, exec, s[0:1]
	s_waitcnt vmcnt(6)
	s_and_saveexec_b64 s[0:1], vcc
	s_cbranch_execz .LBB0_1280
	ds_write_b16 v169, v26 offset:34834
	ds_write_b16_d16_hi v169, v26 offset:35106
	ds_write_b16 v169, v27 offset:35378
	ds_write_b16_d16_hi v169, v27 offset:35650
	ds_write_b16 v169, v28 offset:35922
	ds_write_b16_d16_hi v169, v28 offset:36194
	ds_write_b16 v169, v29 offset:36466
	ds_write_b16_d16_hi v169, v29 offset:36738
.LBB0_1280:
	s_or_b64 exec, exec, s[0:1]
	s_waitcnt vmcnt(5)
	s_and_saveexec_b64 s[0:1], vcc
	s_cbranch_execz .LBB0_1282
	ds_write_b16 v169, v22 offset:34836
	ds_write_b16_d16_hi v169, v22 offset:35108
	ds_write_b16 v169, v23 offset:35380
	ds_write_b16_d16_hi v169, v23 offset:35652
	ds_write_b16 v169, v24 offset:35924
	ds_write_b16_d16_hi v169, v24 offset:36196
	ds_write_b16 v169, v25 offset:36468
	ds_write_b16_d16_hi v169, v25 offset:36740
.LBB0_1282:
	s_or_b64 exec, exec, s[0:1]
	s_waitcnt vmcnt(4)
	s_and_saveexec_b64 s[0:1], vcc
	s_cbranch_execz .LBB0_1284
	ds_write_b16 v169, v18 offset:34838
	ds_write_b16_d16_hi v169, v18 offset:35110
	ds_write_b16 v169, v19 offset:35382
	ds_write_b16_d16_hi v169, v19 offset:35654
	ds_write_b16 v169, v20 offset:35926
	ds_write_b16_d16_hi v169, v20 offset:36198
	ds_write_b16 v169, v21 offset:36470
	ds_write_b16_d16_hi v169, v21 offset:36742
.LBB0_1284:
	s_or_b64 exec, exec, s[0:1]
	s_waitcnt vmcnt(3)
	s_and_saveexec_b64 s[0:1], vcc
	s_cbranch_execz .LBB0_1286
	ds_write_b16 v169, v14 offset:34840
	ds_write_b16_d16_hi v169, v14 offset:35112
	ds_write_b16 v169, v15 offset:35384
	ds_write_b16_d16_hi v169, v15 offset:35656
	ds_write_b16 v169, v16 offset:35928
	ds_write_b16_d16_hi v169, v16 offset:36200
	ds_write_b16 v169, v17 offset:36472
	ds_write_b16_d16_hi v169, v17 offset:36744
.LBB0_1286:
	s_or_b64 exec, exec, s[0:1]
	s_waitcnt vmcnt(2)
	s_and_saveexec_b64 s[0:1], vcc
	s_cbranch_execz .LBB0_1288
	ds_write_b16 v169, v10 offset:34842
	ds_write_b16_d16_hi v169, v10 offset:35114
	ds_write_b16 v169, v11 offset:35386
	ds_write_b16_d16_hi v169, v11 offset:35658
	ds_write_b16 v169, v12 offset:35930
	ds_write_b16_d16_hi v169, v12 offset:36202
	ds_write_b16 v169, v13 offset:36474
	ds_write_b16_d16_hi v169, v13 offset:36746
.LBB0_1288:
	s_or_b64 exec, exec, s[0:1]
	s_waitcnt vmcnt(1)
	s_and_saveexec_b64 s[0:1], vcc
	s_cbranch_execz .LBB0_1290
	ds_write_b16 v169, v6 offset:34844
	ds_write_b16_d16_hi v169, v6 offset:35116
	ds_write_b16 v169, v7 offset:35388
	ds_write_b16_d16_hi v169, v7 offset:35660
	ds_write_b16 v169, v8 offset:35932
	ds_write_b16_d16_hi v169, v8 offset:36204
	ds_write_b16 v169, v9 offset:36476
	ds_write_b16_d16_hi v169, v9 offset:36748
.LBB0_1290:
	s_or_b64 exec, exec, s[0:1]
	s_waitcnt vmcnt(0)
	s_and_saveexec_b64 s[0:1], vcc
	s_cbranch_execz .LBB0_1292
	ds_write_b16 v169, v2 offset:34846
	ds_write_b16_d16_hi v169, v2 offset:35118
	ds_write_b16 v169, v3 offset:35390
	ds_write_b16_d16_hi v169, v3 offset:35662
	ds_write_b16 v169, v4 offset:35934
	ds_write_b16_d16_hi v169, v4 offset:36206
	ds_write_b16 v169, v5 offset:36478
	ds_write_b16_d16_hi v169, v5 offset:36750

; __device__ __forceinline__ void sgu_unit(const Params& p, int l, int un, LAS unsigned char* lds) {
;     ...
;     const float* Wg = p.in[I_SGUW] + ((size_t)l * 4 + h) * 128 * 128;
;     f32x4 wq[8]; u32x4 vv[16];
; #pragma unroll
;     for (int i = 0; i < 8; ++i) wq[i] = *(const f32x4*)(Wg + (i * 512 + tid) * 4);
; #pragma unroll
;     for (int qi = 0; qi < 16; ++qi) vv[qi] = *(const u32x4*)(P + (size_t)(row0 + wave * 16 + qi) * INP + C_SGU_V + lane * 8);
; __global__ void __launch_bounds__(512, 2) fwd(Params p) {
;     ...
;             if (c < (l == 0 ? 72 : 64) || G != 256) pg8::gemm_phase(lds, pg8::Desc{512, 512, 512}, S, E);
;             else { const int un = (l == 0 ? 128 + (c - 72) : 160 + (c - 64)); if (un < (l == 0 ? B_SGU : 256)) sgu_unit(p, l, un, lds); }
.LBB0_1393:
	s_andn2_b64 vcc, exec, s[0:1]
	s_cbranch_vccnz .LBB0_1501
	v_readlane_b32 s0, v252, 5
	v_readlane_b32 s1, v252, 6
	s_lshl_b32 s4, s0, 9
	v_readlane_b32 s0, v252, 20
	v_readlane_b32 s1, v252, 21
	s_and_b64 s[0:1], s[0:1], exec
	s_cselect_b32 s0, 0x48, 64
	s_cmp_ge_i32 s92, s0
	v_readlane_b32 s12, v255, 40
	s_cselect_b64 s[2:3], -1, 0
	v_readlane_b32 s13, v255, 41
	s_and_b64 s[2:3], s[12:13], s[2:3]
	s_mov_b64 s[0:1], -1
	s_and_b64 vcc, exec, s[2:3]
	s_cbranch_vccz .LBB0_1430
	v_readlane_b32 s2, v252, 20
	v_readlane_b32 s3, v252, 21
	s_and_b64 s[0:1], s[2:3], exec
	s_cselect_b32 s0, 56, 0x60
	s_add_i32 s0, s0, s92
	s_and_b64 s[2:3], s[2:3], exec
	s_movk_i32 s1, 0x120
	s_cselect_b32 s1, s1, 0x100
	s_cmp_ge_u32 s0, s1
	s_cbranch_scc1 .LBB0_1429
	v_readlane_b32 s44, v251, 16
	s_lshl_b32 s12, s0, 5
	v_readlane_b32 s0, v253, 39
	v_readlane_b32 s48, v251, 20
	v_readlane_b32 s49, v251, 21
	s_or_b32 s40, s4, s0
	s_mov_b32 s41, s5
	v_readlane_b32 s50, v251, 22
	v_readlane_b32 s51, v251, 23
	v_readlane_b32 s52, v251, 24
	v_readlane_b32 s53, v251, 25
	v_readlane_b32 s54, v251, 26
	v_readlane_b32 s55, v251, 27
	s_mov_b64 s[16:17], s[48:49]
	s_lshl_b64 s[0:1], s[40:41], 9
	s_mov_b64 s[18:19], s[50:51]
	s_waitcnt vmcnt(0)
	v_mov_b32_e32 v64, v0
	s_add_u32 s2, s18, s0
	s_addc_u32 s3, s19, s1
	v_lshlrev_b32_e32 v2, 2, v64
	v_ashrrev_i32_e32 v3, 31, v2
	v_add_u32_e32 v62, 0x800, v2
	s_mov_b64 s[14:15], 0
	v_lshl_add_u64 v[4:5], v[2:3], 2, s[2:3]
	v_ashrrev_i32_e32 v63, 31, v62
	v_lshl_add_u64 v[6:7], v[62:63], 2, s[2:3]
	global_load_dwordx4 v[66:69], v[4:5], off
	global_load_dwordx4 v[70:73], v[6:7], off
	v_add_u32_e32 v102, 0x1000, v2
	v_ashrrev_i32_e32 v103, 31, v102
	v_add_u32_e32 v104, 0x1800, v2
	v_lshl_add_u64 v[4:5], v[102:103], 2, s[2:3]
	v_ashrrev_i32_e32 v105, 31, v104
	v_lshl_add_u64 v[6:7], v[104:105], 2, s[2:3]
	global_load_dwordx4 v[74:77], v[4:5], off
	global_load_dwordx4 v[78:81], v[6:7], off
	s_and_b32 s12, s12, 0x7fffff80
	s_lshl_b64 s[0:1], s[4:5], 2
	v_readlane_b32 s13, v253, 41
	v_add_u32_e32 v106, 0x2000, v2
	s_add_u32 s0, s13, s0
	v_readlane_b32 s13, v253, 42
	v_ashrrev_i32_e32 v107, 31, v106
	v_add_u32_e32 v108, 0x2800, v2
	s_addc_u32 s1, s13, s1
	v_lshl_add_u64 v[4:5], v[106:107], 2, s[2:3]
	v_ashrrev_i32_e32 v109, 31, v108
	s_add_u32 s36, s84, s14
	v_lshl_add_u64 v[6:7], v[108:109], 2, s[2:3]
	global_load_dwordx4 v[82:85], v[4:5], off
	global_load_dwordx4 v[86:89], v[6:7], off
	s_addc_u32 s37, s85, s15
	v_add_u32_e32 v110, 0x3000, v2
	v_add_u32_e32 v112, 0x3800, v2
	s_add_u32 s38, s36, 0x1f1b8000
	v_ashrrev_i32_e32 v111, 31, v110
	v_ashrrev_i32_e32 v113, 31, v112
	v_ashrrev_i32_e32 v103, 6, v64
	s_addc_u32 s39, s37, 0
	v_lshl_add_u64 v[4:5], v[110:111], 2, s[2:3]
	v_lshl_add_u64 v[2:3], v[112:113], 2, s[2:3]
	v_lshlrev_b32_e32 v65, 4, v103
	v_and_b32_e32 v8, 63, v64
	global_load_dwordx4 v[90:93], v[4:5], off
	global_load_dwordx4 v[94:97], v[2:3], off
	v_add_u32_e32 v9, s12, v65
	v_mov_b64_e32 v[2:3], s[38:39]
	s_movk_i32 s13, 0x1e00
	v_mad_i64_i32 v[4:5], s[2:3], v9, s13, v[2:3]
	v_lshlrev_b32_e32 v206, 4, v8
	v_or_b32_e32 v6, 1, v9
	v_lshl_add_u64 v[4:5], v[4:5], 0, v[206:207]
	v_mad_i64_i32 v[6:7], s[2:3], v6, s13, v[2:3]
	v_lshl_add_u64 v[6:7], v[6:7], 0, v[206:207]
	global_load_dwordx4 v[98:101], v[4:5], off offset:1024
	global_load_dwordx4 v[58:61], v[6:7], off offset:1024
	v_or_b32_e32 v4, 2, v9
	v_or_b32_e32 v6, 3, v9
	v_mad_i64_i32 v[4:5], s[2:3], v4, s13, v[2:3]
	v_mad_i64_i32 v[6:7], s[2:3], v6, s13, v[2:3]
	v_lshl_add_u64 v[4:5], v[4:5], 0, v[206:207]
	v_lshl_add_u64 v[6:7], v[6:7], 0, v[206:207]
	global_load_dwordx4 v[54:57], v[4:5], off offset:1024
	global_load_dwordx4 v[50:53], v[6:7], off offset:1024
	v_or_b32_e32 v4, 4, v9
	v_or_b32_e32 v6, 5, v9
	v_mad_i64_i32 v[4:5], s[2:3], v4, s13, v[2:3]
	v_mad_i64_i32 v[6:7], s[2:3], v6, s13, v[2:3]
	v_lshl_add_u64 v[4:5], v[4:5], 0, v[206:207]
	v_lshl_add_u64 v[6:7], v[6:7], 0, v[206:207]
	global_load_dwordx4 v[46:49], v[4:5], off offset:1024
	global_load_dwordx4 v[42:45], v[6:7], off offset:1024
	v_or_b32_e32 v4, 6, v9
	v_or_b32_e32 v6, 7, v9
	v_mad_i64_i32 v[4:5], s[2:3], v4, s13, v[2:3]
	v_mad_i64_i32 v[6:7], s[2:3], v6, s13, v[2:3]
	v_lshl_add_u64 v[4:5], v[4:5], 0, v[206:207]
	v_lshl_add_u64 v[6:7], v[6:7], 0, v[206:207]
	global_load_dwordx4 v[38:41], v[4:5], off offset:1024
	global_load_dwordx4 v[34:37], v[6:7], off offset:1024
	v_or_b32_e32 v4, 8, v9
	v_or_b32_e32 v6, 9, v9
	v_mad_i64_i32 v[4:5], s[2:3], v4, s13, v[2:3]
	v_mad_i64_i32 v[6:7], s[2:3], v6, s13, v[2:3]
	v_lshl_add_u64 v[4:5], v[4:5], 0, v[206:207]
	v_lshl_add_u64 v[6:7], v[6:7], 0, v[206:207]
	global_load_dwordx4 v[30:33], v[4:5], off offset:1024
	global_load_dwordx4 v[26:29], v[6:7], off offset:1024
	v_or_b32_e32 v4, 10, v9
	v_or_b32_e32 v6, 11, v9
	v_mad_i64_i32 v[4:5], s[2:3], v4, s13, v[2:3]
	v_mad_i64_i32 v[6:7], s[2:3], v6, s13, v[2:3]
	v_lshl_add_u64 v[4:5], v[4:5], 0, v[206:207]
	v_lshl_add_u64 v[6:7], v[6:7], 0, v[206:207]
	global_load_dwordx4 v[22:25], v[4:5], off offset:1024
	global_load_dwordx4 v[18:21], v[6:7], off offset:1024
	v_or_b32_e32 v4, 12, v9
	v_or_b32_e32 v6, 13, v9
	v_mad_i64_i32 v[4:5], s[2:3], v4, s13, v[2:3]
	v_mad_i64_i32 v[6:7], s[2:3], v6, s13, v[2:3]
	v_lshl_add_u64 v[4:5], v[4:5], 0, v[206:207]
	v_lshl_add_u64 v[6:7], v[6:7], 0, v[206:207]
	v_lshlrev_b32_e32 v105, 3, v64
	global_load_dwordx4 v[14:17], v[4:5], off offset:1024
	global_load_dwordx4 v[10:13], v[6:7], off offset:1024
	v_or_b32_e32 v4, 14, v9
	v_or_b32_e32 v6, 15, v9
	v_and_b32_e32 v63, 0xf8, v105
	v_mad_i64_i32 v[4:5], s[2:3], v4, s13, v[2:3]
	v_mad_i64_i32 v[2:3], s[2:3], v6, s13, v[2:3]
	v_add_u32_e32 v114, 0, v63
	v_bfe_i32 v63, v64, 5, 25
	s_movk_i32 s13, 0x110
	v_lshl_add_u64 v[4:5], v[4:5], 0, v[206:207]
	v_lshl_add_u64 v[2:3], v[2:3], 0, v[206:207]
	s_waitcnt vmcnt(21)
; #define LAS __attribute__((address_space(3)))
; __device__ __forceinline__ unsigned cvt_pk_bf16(float lo, float hi) { const f32x2 v = {lo, hi}; const bf16x2_t b = __builtin_convertvector(v, bf16x2_t); return __builtin_bit_cast(unsigned, b); }
; __device__ __forceinline__ float bflo(unsigned w) { return __uint_as_float(w << 16); }
; __device__ __forceinline__ float bfhi(unsigned w) { return __uint_as_float(w & 0xffff0000u); }
; __device__ __forceinline__ unsigned short f2bf(float f) { return (unsigned short)(cvt_pk_bf16(f, 0.f) & 0xffffu); }
; __device__ __forceinline__ void sgu_unit(const Params& p, int l, int un, LAS unsigned char* lds) {
;     ...
;     for (int i = 0; i < 8; ++i) { const int e4 = (i * 512 + tid) * 4, r = e4 >> 7, c = e4 & 127; const f32x4 v = wq[i];
;         u32x2 w; w.x = cvt_pk_bf16(v[0], v[1]); w.y = cvt_pk_bf16(v[2], v[3]); *(LAS u32x2*)(Wl + r * 136 + c) = w; }
; #pragma unroll
;     for (int qi = 0; qi < 16; ++qi) { const int q = wave * 16 + qi;
;         const u32x4 v = vv[qi]; float f[8] = {bflo(v.x), bfhi(v.x), bflo(v.y), bfhi(v.y), bflo(v.z), bfhi(v.z), bflo(v.w), bfhi(v.w)}; float ss = 0.f;
; #pragma unroll
;         for (int j = 0; j < 8; ++j) { f[j] = gelu_tanh(f[j]); ss += f[j] * f[j]; }
;         ss = wave_sum(ss); const float rinv = rsqrtf(ss * (1.0f / 512.0f) + EPS);
;         if ((lane >> 4) == h) { const int c0 = (lane & 15) * 8; const float* g = p.in[I_SGUNG] + l * 512 + h * 128 + c0;
; #pragma unroll
;             for (int j = 0; j < 8; ++j) Vl[(c0 + j) * 136 + q] = f2bf(f[j] * rinv * g[j]); } }
	v_cvt_pk_bf16_f32 v66, v66, v67
	v_cvt_pk_bf16_f32 v67, v68, v69
	v_mad_u64_u32 v[68:69], s[2:3], v63, s13, v[114:115]
	global_load_dwordx4 v[6:9], v[4:5], off offset:1024
	s_nop 0
	global_load_dwordx4 v[2:5], v[2:3], off offset:1024
	ds_write_b64 v68, v[66:67]
	v_ashrrev_i32_e32 v66, 7, v62
	s_waitcnt vmcnt(22)
	v_cvt_pk_bf16_f32 v62, v70, v71
	v_cvt_pk_bf16_f32 v63, v72, v73
	v_mad_u64_u32 v[66:67], s[2:3], v66, s13, v[114:115]
	ds_write_b64 v66, v[62:63]
	v_ashrrev_i32_e32 v66, 7, v102
	s_waitcnt vmcnt(21)
	v_cvt_pk_bf16_f32 v62, v74, v75
	v_cvt_pk_bf16_f32 v63, v76, v77
	v_mad_u64_u32 v[66:67], s[2:3], v66, s13, v[114:115]
	ds_write_b64 v66, v[62:63]
	v_ashrrev_i32_e32 v66, 7, v104
	s_waitcnt vmcnt(20)
	v_cvt_pk_bf16_f32 v62, v78, v79
	v_cvt_pk_bf16_f32 v63, v80, v81
	v_mad_u64_u32 v[66:67], s[2:3], v66, s13, v[114:115]
	ds_write_b64 v66, v[62:63]
	v_ashrrev_i32_e32 v66, 7, v106
	s_waitcnt vmcnt(19)
	v_cvt_pk_bf16_f32 v62, v82, v83
	v_cvt_pk_bf16_f32 v63, v84, v85
	v_mad_u64_u32 v[66:67], s[2:3], v66, s13, v[114:115]
	ds_write_b64 v66, v[62:63]
	v_ashrrev_i32_e32 v66, 7, v108
	s_waitcnt vmcnt(18)
	v_cvt_pk_bf16_f32 v62, v86, v87
	v_cvt_pk_bf16_f32 v63, v88, v89
	v_mad_u64_u32 v[66:67], s[2:3], v66, s13, v[114:115]
	ds_write_b64 v66, v[62:63]
	v_ashrrev_i32_e32 v66, 7, v110
	s_waitcnt vmcnt(17)
	v_cvt_pk_bf16_f32 v62, v90, v91
	v_cvt_pk_bf16_f32 v63, v92, v93
	v_mad_u64_u32 v[66:67], s[2:3], v66, s13, v[114:115]
	ds_write_b64 v66, v[62:63]
	v_ashrrev_i32_e32 v66, 7, v112
	v_mad_u64_u32 v[66:67], s[2:3], v66, s13, v[114:115]
	s_waitcnt vmcnt(15)
	v_cvt_pk_bf16_f32 v62, v94, v95
	v_cvt_pk_bf16_f32 v63, v96, v97
	ds_write_b64 v66, v[62:63]
	v_and_b32_e32 v62, 64, v249
	v_add_u32_e32 v62, 64, v62
	v_xor_b32_e32 v63, 32, v249
	v_cmp_lt_i32_e32 vcc, v63, v62
	v_cndmask_b32_e32 v63, v249, v63, vcc
	v_lshlrev_b32_e32 v68, 2, v63
	v_and_b32_e32 v84, 0x78, v105
	v_readlane_b32 s2, v253, 40
	v_lshlrev_b32_e32 v206, 2, v84
	v_readlane_b32 s45, v251, 17
	v_readlane_b32 s46, v251, 18
	v_readlane_b32 s47, v251, 19
	v_readlane_b32 s56, v251, 28
	v_readlane_b32 s57, v251, 29
	v_readlane_b32 s58, v251, 30
	v_readlane_b32 s59, v251, 31
	v_bfe_u32 v66, v64, 4, 2
	v_cmp_eq_u32_e32 vcc, s2, v66
	s_mov_b64 s[20:21], s[52:53]
	v_lshl_add_u32 v67, v103, 5, 0
	v_lshl_add_u64 v[62:63], s[0:1], 0, v[206:207]
	v_mad_u32_u24 v67, v84, s13, v67
	v_lshrrev_b32_e32 v170, 6, v0
	v_lshlrev_b32_e32 v170, 1, v170
	v_and_b32_e32 v171, 15, v0
	v_xor_b32_e32 v168, v170, v171
	v_sub_u32_e32 v168, v168, v170
	v_lshl_add_u32 v168, v168, 4, v67
	v_or_b32_e32 v170, 1, v170
	v_xor_b32_e32 v169, v170, v171
	v_sub_u32_e32 v169, v169, v170
	v_lshl_add_u32 v169, v169, 4, v67
	s_mov_b64 s[22:23], s[54:55]
	s_and_saveexec_b64 s[0:1], vcc
	s_cbranch_execz .LBB0_1398
	ds_write_b16 v168, v98 offset:34816
	ds_write_b16_d16_hi v168, v98 offset:35088
	ds_write_b16 v168, v99 offset:35360
	ds_write_b16_d16_hi v168, v99 offset:35632
	ds_write_b16 v168, v100 offset:35904
	ds_write_b16_d16_hi v168, v100 offset:36176
	ds_write_b16 v168, v101 offset:36448
	ds_write_b16_d16_hi v168, v101 offset:36720
